# code placement trial (doc 9.3): in-projection / MLA up-projection block shifted by 4 bytes, everything after it kept at the same byte phase
# speedup vs baseline: 1.0004x; 1.0004x over previous
; __device__ __forceinline__ size_t ws_wt1(int l) { return (l & 1) ? WS_WS1 : WS_WT1; }
;     __device__ void init(int Mrows, int N, int G, int c, int wgm = 8) { T.init(Mrows / BM, N / BM, G, c, wgm); }
;     __device__ void init(int Mrows, int N, int G, int c) { T.init(Mrows / BM, N / 128, G, c); }
;     __device__ void init(int G, int c, int wgm = 8) { T.init(M / 256, 4, G, c, wgm); }
;     __device__ void init(int G, int c, int wgm) { T.init(M / g8::BM, 4, G, c, wgm); }
; __device__ __forceinline__ KA kargs() { KA p = (KA)__builtin_amdgcn_kernarg_segment_ptr(); asm volatile("" : "+s"(p)); return p; }
; __global__ void __launch_bounds__(NTHR, 2) mk_fwd(Args args) {
;     ...
;         if (RUN(PH_INPROJ)) {
;             const Frame F = make_frame(lds, wv); const KA a = kargs();
;             { g8::DenseSched<D, D, D> S; S.init(M, HP, F.G, (int)blockIdx.x, WGM_INPROJ);
;               EpiInproj E{(bf16_t*)(F.ws + WS_H), (float*)(F.ctl + CW_SSQ), F.ctl + CW_KMAX + l * 16};
;               g8::gemm_phase<D, D>(F.lds, F.wave, F.lane, (const char*)(F.ws + WS_XB), (const char*)(F.ws + ws_wt1(l)), S, E); }
.LBB0_354:
	s_nop 0
	v_readlane_b32 s40, v254, 62
	s_cmp_ge_i32 s1, s40
	s_cselect_b64 s[6:7], -1, 0
	s_and_b64 s[2:3], s[6:7], s[10:11]
	s_andn2_b64 vcc, exec, s[2:3]
	s_mov_b32 s94, s72
	v_readlane_b32 s41, v254, 63
	v_readlane_b32 s42, v255, 0
	v_readlane_b32 s43, v255, 1
	s_cbranch_vccnz .LBB0_460
	v_readlane_b32 s10, v253, 0
	v_readlane_b32 s11, v253, 1
	s_mov_b64 s[40:41], s[10:11]
	s_mov_b32 s2, -1
	s_mov_b64 s[34:35], 0
	v_readlane_b32 s10, v254, 0
	v_readlane_b32 s11, v254, 1
	s_andn2_b64 vcc, exec, s[10:11]
	s_mov_b64 s[16:17], 0
	s_waitcnt lgkmcnt(0)
	v_cndmask_b32_e64 v0, 0, 1, s[10:11]
	v_cmp_ne_u32_e64 s[38:39], 1, v0
	s_cbranch_vccnz .LBB0_357
	v_readlane_b32 s34, v254, 35
	v_readlane_b32 s16, v254, 33
	v_readlane_b32 s62, v254, 31
	v_readlane_b32 s35, v254, 36
	v_readlane_b32 s17, v254, 34
	v_readlane_b32 s61, v254, 32

; __device__ __forceinline__ KA kargs() { KA p = (KA)__builtin_amdgcn_kernarg_segment_ptr(); asm volatile("" : "+s"(p)); return p; }
; __device__ __forceinline__ void claim_fire(unsigned* ctr, int tid, int* pend) { if (tid == 0) *pend = (int)__hip_atomic_fetch_add(ctr, 1u, __ATOMIC_RELAXED, __HIP_MEMORY_SCOPE_AGENT); }
;     const Frame F = make_frame(lds, wv); const KA a = kargs();
;     const int* pos = (const int*)a->in[1];
;     unsigned* q0ctr = F.ctl + CW_QUEUE + ((l + qlo) * 8 + 0 + qs) * 64; unsigned* q1ctr = F.ctl + CW_QUEUE + ((l + qlo) * 8 + 1 + qs) * 64;
;     const bf16_t* QA = (const bf16_t*)(F.ws + WS_QA); const bf16_t* KAp = (const bf16_t*)(F.ws + WS_KA); const bf16_t* VAp = (const bf16_t*)(F.ws + WS_VA);
;     bf16_t* O = (bf16_t*)(F.ws + WS_O);
;     int pend = 0, lastm = 1 << 20;
;     at::claim_fire(q0ctr, F.tid, &pend);
; __global__ void __launch_bounds__(NTHR, 2) mk_fwd(Args args) {
;     ...
;         if (RUN(PH_ATTN1)) phase_attn1(lds, wv, l);
.LBB0_797:
	s_nop 0
	s_nop 0
	s_nop 0
	s_nop 0
	s_nop 0
	s_nop 0
	s_nop 0
	s_nop 0
	s_nop 0
	s_nop 0
	s_nop 0
	s_nop 0
	v_readlane_b32 s1, v255, 2
	v_readlane_b32 s40, v254, 62
	s_or_b32 s1, s1, 3
	v_readlane_b32 s41, v254, 63
	s_cmp_lt_i32 s1, s41
	s_cselect_b64 s[10:11], -1, 0
	s_and_b64 s[2:3], s[6:7], s[10:11]
	s_andn2_b64 vcc, exec, s[2:3]
	v_readlane_b32 s42, v255, 0
	v_readlane_b32 s43, v255, 1
	s_cbranch_vccnz .LBB0_853
	v_readlane_b32 s2, v253, 9
	v_readlane_b32 s3, v253, 10
	s_andn2_b64 vcc, exec, s[2:3]
	s_mov_b64 s[14:15], 0
	s_cbranch_vccnz .LBB0_800
	s_mov_b32 s2, -1
	s_waitcnt lgkmcnt(0)
	v_mbcnt_lo_u32_b32 v0, s2, 0
	v_mbcnt_hi_u32_b32 v0, s2, v0
	v_cmp_eq_u32_e32 vcc, 0, v0
	s_and_b64 s[14:15], vcc, exec
